# v16 + gate/up GEMM: 1/64 weight scale folded into the MFMA block scale (E8M0 0x79, exact), per-element W8INV multiplies and pairing copies removed from the silu*up epilogue (copy propagation + DCE, ha
# baseline (speedup 1.0000x reference)
.LBB0_1935:
	s_add_u32 s48, s14, 0x2f1c8000
	v_readlane_b32 s8, v252, 10
	v_mov_b32_e32 v178, v181
	v_mov_b32_e32 v179, 0
	s_addc_u32 s49, s15, 0
	s_lshl_b32 s8, s8, 5
	s_waitcnt vmcnt(4)
	s_barrier
	s_mov_b64 s[12:13], 0x80
	v_lshl_add_u64 v[4:5], s[36:37], 0, v[178:179]
	s_and_b32 s51, s8, 0x60
	s_add_i32 m0, s31, 0x18000
	v_lshl_add_u64 v[4:5], v[4:5], 0, s[12:13]
	v_mov_b32_e32 v178, v183
	s_lshl_b32 s50, s5, 6
	s_lshl_b32 s5, s5, 13
	s_lshr_b32 s8, s51, 3
	global_load_lds_dwordx4 v[4:5], off
	s_add_i32 m0, s31, 0x1a000
	v_lshl_add_u64 v[4:5], s[36:37], 0, v[178:179]
	v_lshl_add_u64 v[4:5], v[4:5], 0, s[12:13]
	s_add_u32 s14, s14, 0x249c8080
	global_load_lds_dwordx4 v[4:5], off
	s_addc_u32 s15, s15, 0
	v_mov_b32_e32 v4, v184
	s_add_i32 s52, s31, 0x8000
	s_mov_b32 m0, s52
	s_add_i32 s53, s31, 0xa000
	global_load_lds_dwordx4 v4, s[14:15]
	v_mov_b32_e32 v4, v185
	s_mov_b32 m0, s53
	v_readlane_b32 s18, v252, 3
	global_load_lds_dwordx4 v4, s[14:15]
	s_add_u32 s14, s36, 0x40080
	v_mov_b32_e32 v4, v181
	s_addc_u32 s15, s37, 0
	s_add_i32 m0, s31, 0x1c000
	v_readlane_b32 s19, v252, 4
	global_load_lds_dwordx4 v4, s[14:15]
	v_mov_b32_e32 v4, v183
	s_add_i32 m0, s31, 0x1e000
	v_and_b32_e32 v5, 48, v176
	global_load_lds_dwordx4 v4, s[14:15]
	v_ashrrev_i32_e32 v4, 6, v176
	v_lshl_add_u32 v6, v4, 10, s5
	v_lshlrev_b32_e32 v7, 6, v176
	s_movk_i32 s5, 0x3c0
	s_load_dwordx2 s[18:19], s[18:19], 0xb8
	v_and_or_b32 v5, v7, s5, v5
	v_readlane_b32 s5, v252, 2
	s_cmpk_lt_u32 s5, 0x100
	v_add_lshl_u32 v4, v4, s8, 10
	s_cselect_b64 s[14:15], -1, 0
	s_lshl_b32 s5, s4, 2
	s_add_i32 s8, 0, 0x21000
	v_lshlrev_b32_e32 v1, 2, v1
	v_lshlrev_b32_e32 v0, 2, v0
	v_lshlrev_b32_e32 v3, 2, v3
	v_lshlrev_b32_e32 v2, 2, v2
	v_lshlrev_b32_e32 v7, 2, v176
	s_add_i32 s54, s8, s5
	s_ashr_i32 s5, s4, 31
	v_add3_u32 v189, s8, v1, v0
	v_add3_u32 v190, s8, v3, v2
	s_add_i32 s8, 0, 0x21200
	v_and_b32_e32 v7, 32, v7
	v_add3_u32 v191, s8, v1, v0
	v_add3_u32 v192, s8, v3, v2
	s_waitcnt lgkmcnt(0)
	s_add_u32 s8, s18, s16
	v_bitop3_b32 v188, v5, v4, v7 bitop3:0xde
	s_waitcnt vmcnt(6)
	s_addc_u32 s17, s19, s17
	v_bitop3_b32 v6, v5, v6, v7 bitop3:0xde
	s_add_u32 s16, s8, 0x249c8080
	v_add_u32_e32 v0, 0, v188
	v_ashrrev_i32_e32 v177, 31, v176
	s_addc_u32 s17, s17, 0
	s_add_i32 s55, 0, 0x20104
	s_lshl_b64 s[18:19], s[4:5], 2
	v_add_u32_e32 v193, 0x10000, v0
	v_add_u32_e32 v194, 0, v6
	v_mov_b32_e32 v195, 0x7f7f7f7f
	v_mov_b32_e32 v250, 0x79797979
	s_add_i32 s5, 0, 0x14000
	s_movk_i32 s56, 0x600
	s_mov_b32 s20, 0x3c800000
	s_mov_b32 s57, 0
	s_mov_b64 s[26:27], s[36:37]
	s_barrier
	s_branch .LBB0_1937
.LBB0_1936:
	v_mbcnt_lo_u32_b32 v0, -1, 0
	v_mbcnt_hi_u32_b32 v0, -1, v0
	s_lshl_b32 s34, s59, 8
	v_ashrrev_i32_e32 v1, 1, v0
	v_bfi_b32 v2, -16, v1, v0
	v_and_b32_e32 v178, 16, v0
	v_mov_b32_e32 v5, v160
	v_mov_b32_e32 v160, v173
	v_mul_f32_e32 v0, 0xbfb8aa3b, v172
	v_exp_f32_e32 v0, v0
	s_add_i32 s34, s34, s50
	s_lshl_b32 s23, s30, 7
	v_add_f32_e32 v0, 1.0, v0
	v_rcp_f32_e32 v3, v0
	v_mul_f32_e32 v0, 0xbfb8aa3b, v173
	v_exp_f32_e32 v8, v0
	s_ashr_i32 s8, s23, 31
	v_mul_f32_e32 v3, v172, v3
	v_mul_f32_e32 v3, v3, v5
	v_add_f32_e32 v4, 1.0, v8
	v_rcp_f32_e32 v10, v4
	v_mov_b32_e32 v5, v162
	v_mov_b32_e32 v162, v175
	v_mul_f32_e32 v8, 0xbfb8aa3b, v174
	v_exp_f32_e32 v11, v8
	v_mul_f32_e32 v6, v173, v10
	s_mul_i32 s30, s34, 0x600
	v_add_f32_e32 v10, 1.0, v11
	v_rcp_f32_e32 v10, v10
	v_mul_f32_e32 v12, 0xbfb8aa3b, v175
	v_exp_f32_e32 v12, v12
	s_mul_hi_i32 s35, s34, 0x600
	v_mul_f32_e32 v4, v174, v10
	v_mul_f32_e32 v10, v4, v5
	v_add_f32_e32 v11, 1.0, v12
	v_mul_f32_e32 v12, v6, v161
	v_mov_b32_e32 v7, v152
	v_rcp_f32_e32 v11, v11
	v_mul_f32_e32 v4, 0xbfb8aa3b, v168
	v_exp_f32_e32 v5, v4
	v_mov_b32_e32 v4, v179
	v_cvt_pk_fp8_f32 v4, v3, v12
	v_mul_f32_e32 v8, v175, v11
	v_add_f32_e32 v3, 1.0, v5
	v_rcp_f32_e32 v3, v3
	v_mov_b32_e32 v152, v169
	v_mul_f32_e32 v11, v8, v163
	v_mul_f32_e32 v3, v168, v3
	v_mul_f32_e32 v5, 0xbfb8aa3b, v169
	v_exp_f32_e32 v5, v5
	v_mul_f32_e32 v3, v3, v7
	v_mov_b32_e32 v7, v154
	v_cvt_pk_fp8_f32 v4, v10, v11 op_sel:[0,0,1]
	v_mul_f32_e32 v10, 0xbfb8aa3b, v170
	v_mov_b32_e32 v154, v171
	v_add_f32_e32 v5, 1.0, v5
	v_exp_f32_e32 v12, v10
	v_rcp_f32_e32 v5, v5
	v_mul_f32_e32 v13, 0xbfb8aa3b, v171
	v_exp_f32_e32 v13, v13
	s_add_u32 s36, s48, s30
	v_mul_f32_e32 v5, v169, v5
	v_add_f32_e32 v8, 1.0, v12
	v_rcp_f32_e32 v8, v8
	v_add_f32_e32 v12, 1.0, v13
	v_rcp_f32_e32 v12, v12
	v_mul_f32_e32 v9, v5, v153
	v_mul_f32_e32 v5, v170, v8
	v_mul_f32_e32 v13, v5, v7
	v_mul_f32_e32 v5, v171, v12
	v_mul_f32_e32 v10, v5, v155
	v_mov_b32_e32 v5, v179
	v_mov_b32_e32 v7, v148
	v_mov_b32_e32 v148, v165
	v_cvt_pk_fp8_f32 v5, v3, v9
	v_mul_f32_e32 v11, 0xbfb8aa3b, v165
	v_exp_f32_e32 v11, v11
	v_mul_f32_e32 v3, 0xbfb8aa3b, v164
	v_exp_f32_e32 v3, v3
	v_cvt_pk_fp8_f32 v5, v13, v10 op_sel:[0,0,1]
	v_add_f32_e32 v10, 1.0, v11
	v_rcp_f32_e32 v12, v10
	v_mov_b32_e32 v11, v150
	v_add_f32_e32 v3, 1.0, v3
	v_rcp_f32_e32 v3, v3
	v_mul_f32_e32 v13, 0xbfb8aa3b, v166
	v_exp_f32_e32 v13, v13
	v_mov_b32_e32 v150, v167
	v_mul_f32_e32 v3, v164, v3
	v_mul_f32_e32 v3, v3, v7
	v_add_f32_e32 v7, 1.0, v13
	v_mul_f32_e32 v6, v165, v12
	v_rcp_f32_e32 v7, v7
	v_mul_f32_e32 v14, v6, v149
	v_mul_f32_e32 v8, 0xbfb8aa3b, v167
	v_exp_f32_e32 v8, v8
	v_mul_f32_e32 v6, v166, v7
	v_mul_f32_e32 v10, v6, v11
	v_add_f32_e32 v11, 1.0, v8
	v_mov_b32_e32 v9, v144
	v_rcp_f32_e32 v11, v11
	v_mul_f32_e32 v6, 0xbfb8aa3b, v156
	v_exp_f32_e32 v7, v6
	v_mov_b32_e32 v6, v179
	v_cvt_pk_fp8_f32 v6, v3, v14
	v_mov_b32_e32 v144, v157
	v_add_f32_e32 v3, 1.0, v7
	v_rcp_f32_e32 v3, v3
	v_mul_f32_e32 v7, v167, v11
	v_mul_f32_e32 v7, v7, v151
	v_mov_b32_e32 v13, v146
	v_cvt_pk_fp8_f32 v6, v10, v7 op_sel:[0,0,1]
	v_mul_f32_e32 v3, v156, v3
	v_mul_f32_e32 v8, 0xbfb8aa3b, v158
	v_mul_f32_e32 v7, 0xbfb8aa3b, v157
	v_exp_f32_e32 v8, v8
	v_exp_f32_e32 v7, v7
	v_mov_b32_e32 v146, v159
	v_mul_f32_e32 v3, v3, v9
	v_add_f32_e32 v8, 1.0, v8
	v_add_f32_e32 v7, 1.0, v7
	v_rcp_f32_e32 v14, v8
	v_rcp_f32_e32 v7, v7
	v_mul_f32_e32 v15, 0xbfb8aa3b, v159
	v_exp_f32_e32 v15, v15
	s_addc_u32 s35, s49, s35
	v_mul_f32_e32 v7, v157, v7
	v_mul_f32_e32 v10, v7, v145
	v_add_f32_e32 v7, 1.0, v15
	v_mul_f32_e32 v11, v158, v14
	v_rcp_f32_e32 v12, v7
	v_mov_b32_e32 v7, v179
	v_cvt_pk_fp8_f32 v7, v3, v10
	v_mul_f32_e32 v3, v11, v13
	v_mul_f32_e32 v8, v159, v12
	v_mul_f32_e32 v8, v8, v147
	v_cvt_pk_fp8_f32 v7, v3, v8 op_sel:[0,0,1]
	v_mov_b32_e32 v9, v136
	v_mov_b32_e32 v136, v141
	v_mul_f32_e32 v3, 0xbfb8aa3b, v140
	v_exp_f32_e32 v3, v3
	s_add_u32 s36, s36, s23
	s_addc_u32 s35, s35, s8
	v_mul_f32_e32 v14, 0xbfb8aa3b, v141
	s_add_u32 s36, s36, s51
	v_add_f32_e32 v3, 1.0, v3
	v_exp_f32_e32 v14, v14
	s_addc_u32 s37, s35, 0
	v_rcp_f32_e32 v3, v3
	v_lshl_add_u64 v[0:1], s[36:37], 0, v[178:179]
	v_permlane32_swap_b32_e32 v4, v6
	v_permlane32_swap_b32_e32 v5, v7
	s_nop 1
	v_permlane16_swap_b32_e32 v4, v5
	v_permlane16_swap_b32_e32 v6, v7
	v_mad_i64_i32 v[10:11], s[36:37], v2, s56, v[0:1]
	global_store_dwordx4 v[10:11], v[4:7], off
	v_mul_f32_e32 v3, v140, v3
	v_mul_f32_e32 v3, v3, v9
	v_add_f32_e32 v4, 1.0, v14
	v_rcp_f32_e32 v8, v4
	v_mov_b32_e32 v5, v138
	v_mov_b32_e32 v138, v143
	v_mul_f32_e32 v6, 0xbfb8aa3b, v142
	v_exp_f32_e32 v9, v6
	v_mul_f32_e32 v8, v141, v8
	v_mul_f32_e32 v10, 0xbfb8aa3b, v143
	v_add_f32_e32 v9, 1.0, v9
	v_rcp_f32_e32 v9, v9
	v_exp_f32_e32 v10, v10
	v_mul_f32_e32 v11, v8, v137
	s_addk_i32 s34, 0x80
	v_mul_f32_e32 v4, v142, v9
	v_mul_f32_e32 v12, v4, v5
	v_mov_b32_e32 v9, v128
	v_add_f32_e32 v10, 1.0, v10
	v_mul_f32_e32 v4, 0xbfb8aa3b, v132
	v_exp_f32_e32 v5, v4
	v_rcp_f32_e32 v10, v10
	v_mov_b32_e32 v4, v179
	v_cvt_pk_fp8_f32 v4, v3, v11
	v_add_f32_e32 v3, 1.0, v5
	v_rcp_f32_e32 v3, v3
	v_mul_f32_e32 v6, v143, v10
	v_mov_b32_e32 v128, v133
	v_mul_f32_e32 v10, v6, v139
	v_mul_f32_e32 v3, v132, v3
	v_mul_f32_e32 v5, 0xbfb8aa3b, v133
	v_exp_f32_e32 v5, v5
	v_mul_f32_e32 v3, v3, v9
	v_mov_b32_e32 v9, v130
	v_cvt_pk_fp8_f32 v4, v12, v10 op_sel:[0,0,1]
	v_mul_f32_e32 v10, 0xbfb8aa3b, v134
	v_mov_b32_e32 v130, v135
	v_add_f32_e32 v5, 1.0, v5
	v_exp_f32_e32 v12, v10
	v_rcp_f32_e32 v5, v5
	v_mul_f32_e32 v13, 0xbfb8aa3b, v135
	v_exp_f32_e32 v13, v13
	s_add_i32 s30, s30, 0x30000
	v_mul_f32_e32 v5, v133, v5
	v_add_f32_e32 v6, 1.0, v12
	v_rcp_f32_e32 v6, v6
	v_add_f32_e32 v12, 1.0, v13
	v_rcp_f32_e32 v12, v12
	v_mul_f32_e32 v7, v5, v129
	v_mul_f32_e32 v5, v134, v6
	v_mul_f32_e32 v13, v5, v9
	v_mul_f32_e32 v5, v135, v12
	v_mul_f32_e32 v10, v5, v131
	v_mov_b32_e32 v5, v179
	v_cvt_pk_fp8_f32 v5, v3, v7
	v_mov_b32_e32 v7, v124
	v_mov_b32_e32 v124, v121
	v_mul_f32_e32 v11, 0xbfb8aa3b, v121
	v_exp_f32_e32 v11, v11
	v_mul_f32_e32 v3, 0xbfb8aa3b, v120
	v_exp_f32_e32 v3, v3
	v_cvt_pk_fp8_f32 v5, v13, v10 op_sel:[0,0,1]
	v_add_f32_e32 v10, 1.0, v11
	v_rcp_f32_e32 v12, v10
	v_mov_b32_e32 v11, v126
	v_add_f32_e32 v3, 1.0, v3
	v_rcp_f32_e32 v3, v3
	v_mul_f32_e32 v13, 0xbfb8aa3b, v122
	v_exp_f32_e32 v13, v13
	v_mov_b32_e32 v126, v123
	v_mul_f32_e32 v3, v120, v3
	v_mul_f32_e32 v3, v3, v7
	v_add_f32_e32 v7, 1.0, v13
	v_mul_f32_e32 v6, v121, v12
	v_rcp_f32_e32 v7, v7
	v_mul_f32_e32 v14, v6, v125
	v_mul_f32_e32 v8, 0xbfb8aa3b, v123
	v_exp_f32_e32 v8, v8
	v_mul_f32_e32 v6, v122, v7
	v_mul_f32_e32 v10, v6, v11
	v_add_f32_e32 v11, 1.0, v8
	v_mov_b32_e32 v9, v116
	v_rcp_f32_e32 v11, v11
	v_mul_f32_e32 v6, 0xbfb8aa3b, v112
	v_exp_f32_e32 v7, v6
	v_mov_b32_e32 v6, v179
	v_cvt_pk_fp8_f32 v6, v3, v14
	v_mov_b32_e32 v116, v113
	v_add_f32_e32 v3, 1.0, v7
	v_rcp_f32_e32 v3, v3
	v_mul_f32_e32 v7, v123, v11
	v_mul_f32_e32 v7, v7, v127
	v_mov_b32_e32 v13, v118
	v_cvt_pk_fp8_f32 v6, v10, v7 op_sel:[0,0,1]
	v_mul_f32_e32 v3, v112, v3
	v_mul_f32_e32 v8, 0xbfb8aa3b, v114
	v_mul_f32_e32 v7, 0xbfb8aa3b, v113
	v_exp_f32_e32 v8, v8
	v_exp_f32_e32 v7, v7
	v_mov_b32_e32 v118, v115
	v_mul_f32_e32 v3, v3, v9
	v_add_f32_e32 v8, 1.0, v8
	v_add_f32_e32 v7, 1.0, v7
	v_rcp_f32_e32 v14, v8
	v_rcp_f32_e32 v7, v7
	v_mul_f32_e32 v15, 0xbfb8aa3b, v115
	v_exp_f32_e32 v15, v15
	v_permlane32_swap_b32_e32 v4, v6
	v_mul_f32_e32 v7, v113, v7
	v_mul_f32_e32 v10, v7, v117
	v_add_f32_e32 v7, 1.0, v15
	v_mul_f32_e32 v11, v114, v14
	v_rcp_f32_e32 v12, v7
	v_mov_b32_e32 v7, v179
	v_cvt_pk_fp8_f32 v7, v3, v10
	v_mul_f32_e32 v3, v11, v13
	v_mul_f32_e32 v8, v115, v12
	v_mul_f32_e32 v8, v8, v119
	v_cvt_pk_fp8_f32 v7, v3, v8 op_sel:[0,0,1]
	v_add_u32_e32 v14, 32, v2
	v_mad_i64_i32 v[0:1], s[36:37], v14, s56, v[0:1]
	v_permlane32_swap_b32_e32 v5, v7
	s_nop 1
	v_permlane16_swap_b32_e32 v4, v5
	v_permlane16_swap_b32_e32 v6, v7
	global_store_dwordx4 v[0:1], v[4:7], off
	s_nop 1
	v_mov_b32_e32 v5, v104
	v_mov_b32_e32 v104, v109
	v_mul_f32_e32 v0, 0xbfb8aa3b, v108
	v_exp_f32_e32 v0, v0
	s_mul_hi_i32 s34, s34, 0x600
	s_add_u32 s30, s48, s30
	v_add_f32_e32 v0, 1.0, v0
	v_rcp_f32_e32 v3, v0
	v_mul_f32_e32 v0, 0xbfb8aa3b, v109
	v_exp_f32_e32 v8, v0
	s_addc_u32 s34, s49, s34
	v_mul_f32_e32 v3, v108, v3
	v_mul_f32_e32 v3, v3, v5
	v_add_f32_e32 v4, 1.0, v8
	v_rcp_f32_e32 v10, v4
	v_mov_b32_e32 v5, v106
	v_mov_b32_e32 v106, v111
	v_mul_f32_e32 v8, 0xbfb8aa3b, v110
	v_exp_f32_e32 v11, v8
	v_mul_f32_e32 v6, v109, v10
	s_add_u32 s23, s30, s23
	v_add_f32_e32 v10, 1.0, v11
	v_rcp_f32_e32 v10, v10
	v_mul_f32_e32 v12, 0xbfb8aa3b, v111
	v_exp_f32_e32 v12, v12
	s_addc_u32 s8, s34, s8
	v_mul_f32_e32 v4, v110, v10
	v_mul_f32_e32 v10, v4, v5
	v_add_f32_e32 v11, 1.0, v12
	v_mul_f32_e32 v12, v6, v105
	v_mov_b32_e32 v7, v96
	v_rcp_f32_e32 v11, v11
	v_mul_f32_e32 v4, 0xbfb8aa3b, v100
	v_exp_f32_e32 v5, v4
	v_mov_b32_e32 v4, v179
	v_cvt_pk_fp8_f32 v4, v3, v12
	v_mul_f32_e32 v8, v111, v11
	v_add_f32_e32 v3, 1.0, v5
	v_rcp_f32_e32 v3, v3
	v_mov_b32_e32 v96, v101
	v_mul_f32_e32 v11, v8, v107
	v_mul_f32_e32 v3, v100, v3
	v_mul_f32_e32 v5, 0xbfb8aa3b, v101
	v_exp_f32_e32 v5, v5
	v_mul_f32_e32 v3, v3, v7
	v_mov_b32_e32 v7, v98
	v_cvt_pk_fp8_f32 v4, v10, v11 op_sel:[0,0,1]
	v_mul_f32_e32 v10, 0xbfb8aa3b, v102
	v_mov_b32_e32 v98, v103
	v_add_f32_e32 v5, 1.0, v5
	v_exp_f32_e32 v12, v10
	v_rcp_f32_e32 v5, v5
	v_mul_f32_e32 v13, 0xbfb8aa3b, v103
	v_exp_f32_e32 v13, v13
	s_add_u32 s34, s23, s51
	v_mul_f32_e32 v5, v101, v5
	v_add_f32_e32 v8, 1.0, v12
	v_rcp_f32_e32 v8, v8
	v_add_f32_e32 v12, 1.0, v13
	v_rcp_f32_e32 v12, v12
	v_mul_f32_e32 v9, v5, v97
	v_mul_f32_e32 v5, v102, v8
	v_mul_f32_e32 v13, v5, v7
	v_mul_f32_e32 v5, v103, v12
	v_mul_f32_e32 v10, v5, v99
	v_mov_b32_e32 v5, v179
	v_mov_b32_e32 v7, v88
	v_mov_b32_e32 v88, v93
	v_cvt_pk_fp8_f32 v5, v3, v9
	v_mul_f32_e32 v11, 0xbfb8aa3b, v93
	v_exp_f32_e32 v11, v11
	v_mul_f32_e32 v3, 0xbfb8aa3b, v92
	v_exp_f32_e32 v3, v3
	v_cvt_pk_fp8_f32 v5, v13, v10 op_sel:[0,0,1]
	v_add_f32_e32 v10, 1.0, v11
	v_rcp_f32_e32 v12, v10
	v_mov_b32_e32 v11, v90
	v_add_f32_e32 v3, 1.0, v3
	v_rcp_f32_e32 v3, v3
	v_mul_f32_e32 v13, 0xbfb8aa3b, v94
	v_exp_f32_e32 v13, v13
	v_mov_b32_e32 v90, v95
	v_mul_f32_e32 v3, v92, v3
	v_mul_f32_e32 v3, v3, v7
	v_add_f32_e32 v7, 1.0, v13
	v_mul_f32_e32 v6, v93, v12
	v_rcp_f32_e32 v7, v7
	v_mul_f32_e32 v15, v6, v89
	v_mul_f32_e32 v8, 0xbfb8aa3b, v95
	v_exp_f32_e32 v8, v8
	v_mul_f32_e32 v6, v94, v7
	v_mul_f32_e32 v10, v6, v11
	v_add_f32_e32 v11, 1.0, v8
	v_mov_b32_e32 v9, v80
	v_rcp_f32_e32 v11, v11
	v_mul_f32_e32 v6, 0xbfb8aa3b, v84
	v_exp_f32_e32 v7, v6
	v_mov_b32_e32 v6, v179
	v_cvt_pk_fp8_f32 v6, v3, v15
	v_mov_b32_e32 v80, v85
	v_add_f32_e32 v3, 1.0, v7
	v_rcp_f32_e32 v3, v3
	v_mul_f32_e32 v7, v95, v11
	v_mul_f32_e32 v7, v7, v91
	v_mov_b32_e32 v13, v82
	v_cvt_pk_fp8_f32 v6, v10, v7 op_sel:[0,0,1]
	v_mul_f32_e32 v3, v84, v3
	v_mul_f32_e32 v8, 0xbfb8aa3b, v86
	v_mul_f32_e32 v7, 0xbfb8aa3b, v85
	v_exp_f32_e32 v8, v8
	v_exp_f32_e32 v7, v7
	v_mov_b32_e32 v82, v87
	v_mul_f32_e32 v3, v3, v9
	v_add_f32_e32 v8, 1.0, v8
	v_add_f32_e32 v7, 1.0, v7
	v_rcp_f32_e32 v15, v8
	v_rcp_f32_e32 v7, v7
	v_mul_f32_e32 v16, 0xbfb8aa3b, v87
	v_exp_f32_e32 v16, v16
	s_addc_u32 s35, s8, 0
	v_mul_f32_e32 v7, v85, v7
	v_mul_f32_e32 v10, v7, v81
	v_add_f32_e32 v7, 1.0, v16
	v_mul_f32_e32 v11, v86, v15
	v_rcp_f32_e32 v12, v7
	v_mov_b32_e32 v7, v179
	v_cvt_pk_fp8_f32 v7, v3, v10
	v_mul_f32_e32 v3, v11, v13
	v_mul_f32_e32 v8, v87, v12
	v_mul_f32_e32 v8, v8, v83
	v_cvt_pk_fp8_f32 v7, v3, v8 op_sel:[0,0,1]
	v_mov_b32_e32 v9, v72
	v_mov_b32_e32 v72, v77
	v_mul_f32_e32 v3, 0xbfb8aa3b, v76
	v_exp_f32_e32 v10, v3
	v_lshl_add_u64 v[0:1], s[34:35], 0, v[178:179]
	v_permlane32_swap_b32_e32 v4, v6
	v_add_f32_e32 v10, 1.0, v10
	v_rcp_f32_e32 v12, v10
	v_permlane32_swap_b32_e32 v5, v7
	v_mul_f32_e32 v13, 0xbfb8aa3b, v77
	v_exp_f32_e32 v13, v13
	v_permlane16_swap_b32_e32 v4, v5
	v_permlane16_swap_b32_e32 v6, v7
	v_mad_i64_i32 v[2:3], s[34:35], v2, s56, v[0:1]
	global_store_dwordx4 v[2:3], v[4:7], off
	v_mul_f32_e32 v2, v76, v12
	v_mul_f32_e32 v8, v2, v9
	v_add_f32_e32 v2, 1.0, v13
	v_rcp_f32_e32 v6, v2
	v_mov_b32_e32 v3, v74
	v_mov_b32_e32 v74, v79
	v_mul_f32_e32 v4, 0xbfb8aa3b, v78
	v_exp_f32_e32 v7, v4
	v_mul_f32_e32 v6, v77, v6
	v_mul_f32_e32 v9, 0xbfb8aa3b, v79
	v_add_f32_e32 v7, 1.0, v7
	v_rcp_f32_e32 v7, v7
	v_exp_f32_e32 v9, v9
	v_mul_f32_e32 v10, v6, v73
	v_mad_i64_i32 v[0:1], s[34:35], v14, s56, v[0:1]
	v_mul_f32_e32 v2, v78, v7
	v_mul_f32_e32 v11, v2, v3
	v_mov_b32_e32 v7, v64
	v_add_f32_e32 v9, 1.0, v9
	v_mul_f32_e32 v2, 0xbfb8aa3b, v68
	v_exp_f32_e32 v3, v2
	v_rcp_f32_e32 v9, v9
	v_mov_b32_e32 v64, v69
	v_mov_b32_e32 v2, v179
	v_add_f32_e32 v3, 1.0, v3
	v_mul_f32_e32 v4, v79, v9
	v_rcp_f32_e32 v3, v3
	v_mul_f32_e32 v9, v4, v75
	v_cvt_pk_fp8_f32 v2, v8, v10
	v_mul_f32_e32 v8, 0xbfb8aa3b, v69
	v_exp_f32_e32 v8, v8
	v_mul_f32_e32 v3, v68, v3
	v_mul_f32_e32 v10, v3, v7
	v_mov_b32_e32 v7, v66
	v_add_f32_e32 v3, 1.0, v8
	v_mul_f32_e32 v8, 0xbfb8aa3b, v70
	v_mov_b32_e32 v66, v71
	v_cvt_pk_fp8_f32 v2, v11, v9 op_sel:[0,0,1]
	v_exp_f32_e32 v11, v8
	v_rcp_f32_e32 v3, v3
	v_mul_f32_e32 v12, 0xbfb8aa3b, v71
	v_exp_f32_e32 v12, v12
	s_and_b64 vcc, exec, s[24:25]
	v_mul_f32_e32 v3, v69, v3
	v_add_f32_e32 v4, 1.0, v11
	v_rcp_f32_e32 v4, v4
	v_add_f32_e32 v11, 1.0, v12
	v_rcp_f32_e32 v11, v11
	v_mul_f32_e32 v5, v3, v65
	v_mul_f32_e32 v3, v70, v4
	v_mul_f32_e32 v12, v3, v7
	v_mul_f32_e32 v3, v71, v11
	v_mul_f32_e32 v8, v3, v67
	v_mov_b32_e32 v3, v179
	v_cvt_pk_fp8_f32 v3, v10, v5
	v_mov_b32_e32 v5, v56
	v_mov_b32_e32 v56, v61
	v_mul_f32_e32 v6, 0xbfb8aa3b, v60
	v_exp_f32_e32 v9, v6
	v_cvt_pk_fp8_f32 v3, v12, v8 op_sel:[0,0,1]
	v_mul_f32_e32 v10, 0xbfb8aa3b, v61
	v_exp_f32_e32 v10, v10
	v_add_f32_e32 v8, 1.0, v9
	v_rcp_f32_e32 v11, v8
	v_mov_b32_e32 v9, v58
	v_add_f32_e32 v8, 1.0, v10
	v_rcp_f32_e32 v10, v8
	v_mul_f32_e32 v4, v60, v11
	v_mul_f32_e32 v12, 0xbfb8aa3b, v62
	v_exp_f32_e32 v12, v12
	v_mul_f32_e32 v13, v4, v5
	v_mov_b32_e32 v58, v63
	v_mul_f32_e32 v4, v61, v10
	v_add_f32_e32 v5, 1.0, v12
	v_rcp_f32_e32 v5, v5
	v_mul_f32_e32 v12, v4, v57
	v_mul_f32_e32 v6, 0xbfb8aa3b, v63
	v_exp_f32_e32 v6, v6
	v_mul_f32_e32 v4, v62, v5
	v_mul_f32_e32 v8, v4, v9
	v_add_f32_e32 v9, 1.0, v6
	v_mov_b32_e32 v7, v48
	v_rcp_f32_e32 v9, v9
	v_mul_f32_e32 v4, 0xbfb8aa3b, v52
	v_exp_f32_e32 v5, v4
	v_mov_b32_e32 v4, v179
	v_cvt_pk_fp8_f32 v4, v13, v12
	v_mul_f32_e32 v9, v63, v9
	v_add_f32_e32 v5, 1.0, v5
	v_rcp_f32_e32 v5, v5
	v_mul_f32_e32 v9, v9, v59
	v_mov_b32_e32 v48, v53
	v_mov_b32_e32 v11, v50
	v_cvt_pk_fp8_f32 v4, v8, v9 op_sel:[0,0,1]
	v_mul_f32_e32 v5, v52, v5
	v_mul_f32_e32 v6, 0xbfb8aa3b, v53
	v_mul_f32_e32 v12, 0xbfb8aa3b, v54
	v_exp_f32_e32 v6, v6
	v_exp_f32_e32 v12, v12
	v_mul_f32_e32 v13, v5, v7
	v_mov_b32_e32 v50, v55
	v_add_f32_e32 v5, 1.0, v6
	v_add_f32_e32 v6, 1.0, v12
	v_rcp_f32_e32 v12, v6
	v_mov_b32_e32 v7, v51
	v_rcp_f32_e32 v5, v5
	v_mul_f32_e32 v15, 0xbfb8aa3b, v55
	v_exp_f32_e32 v15, v15
	v_permlane32_swap_b32_e32 v2, v4
	v_mul_f32_e32 v5, v53, v5
	v_mul_f32_e32 v8, v5, v49
	v_add_f32_e32 v5, 1.0, v15
	v_mul_f32_e32 v9, v54, v12
	v_rcp_f32_e32 v10, v5
	v_mov_b32_e32 v5, v179
	v_cvt_pk_fp8_f32 v5, v13, v8
	v_mul_f32_e32 v8, v9, v11
	v_mul_f32_e32 v6, v55, v10
	v_mul_f32_e32 v6, v6, v51
	v_cvt_pk_fp8_f32 v5, v8, v6 op_sel:[0,0,1]
	s_mov_b32 s59, s58
	s_mov_b32 s30, s22
	s_mov_b64 s[36:37], s[26:27]
	v_permlane32_swap_b32_e32 v3, v5
	s_nop 1
	v_permlane16_swap_b32_e32 v2, v3
	v_permlane16_swap_b32_e32 v4, v5
	global_store_dwordx4 v[0:1], v[2:5], off
	s_cbranch_vccnz .LBB0_1947

.LBB0_1944:
	s_add_u32 s40, s36, 0x80
	s_addc_u32 s41, s37, 0
	v_add_u32_e32 v178, s5, v188
	s_and_b64 s[38:39], s[38:39], exec
	ds_read_b128 v[196:199], v178
	ds_read_b128 v[200:203], v178 offset:1024
	ds_read_b128 v[204:207], v178 offset:2048
	ds_read_b128 v[208:211], v178 offset:3072
	v_mov_b32_e32 v178, v181
	s_mov_b32 m0, s43
	s_cselect_b32 s39, s27, s23
	s_cselect_b32 s38, s26, s8
	s_waitcnt lgkmcnt(0)
	v_mfma_scale_f32_16x16x128_f8f6f4 v[172:175], v[0:7], v[40:47], v[172:175], v250, v195 op_sel_hi:[0,0,0]
	global_load_lds_dwordx4 v178, s[38:39]
	v_mov_b32_e32 v178, v183
	s_mov_b32 m0, s44
	s_cselect_b32 s41, s11, s41
	global_load_lds_dwordx4 v178, s[38:39]
	v_mfma_scale_f32_16x16x128_f8f6f4 v[168:171], v[8:15], v[40:47], v[168:171], v250, v195 op_sel_hi:[0,0,0]
	s_barrier
	s_waitcnt lgkmcnt(0)
	s_cselect_b32 s40, s10, s40
	v_mfma_scale_f32_16x16x128_f8f6f4 v[164:167], v[0:7], v[32:39], v[164:167], v250, v195 op_sel_hi:[0,0,0]
	v_mfma_scale_f32_16x16x128_f8f6f4 v[156:159], v[8:15], v[32:39], v[156:159], v250, v195 op_sel_hi:[0,0,0]
	v_mfma_scale_f32_16x16x128_f8f6f4 v[140:143], v[0:7], v[24:31], v[140:143], v250, v195 op_sel_hi:[0,0,0]
	v_mfma_scale_f32_16x16x128_f8f6f4 v[132:135], v[8:15], v[24:31], v[132:135], v250, v195 op_sel_hi:[0,0,0]
	v_mfma_scale_f32_16x16x128_f8f6f4 v[120:123], v[0:7], v[16:23], v[120:123], v250, v195 op_sel_hi:[0,0,0]
	v_mfma_scale_f32_16x16x128_f8f6f4 v[112:115], v[8:15], v[16:23], v[112:115], v250, v195 op_sel_hi:[0,0,0]
	s_setprio 1
	v_mfma_scale_f32_16x16x128_f8f6f4 v[160:163], v[196:203], v[40:47], v[160:163], v250, v195 op_sel_hi:[0,0,0]
	v_mfma_scale_f32_16x16x128_f8f6f4 v[152:155], v[204:211], v[40:47], v[152:155], v250, v195 op_sel_hi:[0,0,0]
	v_mfma_scale_f32_16x16x128_f8f6f4 v[148:151], v[196:203], v[32:39], v[148:151], v250, v195 op_sel_hi:[0,0,0]
	v_mfma_scale_f32_16x16x128_f8f6f4 v[144:147], v[204:211], v[32:39], v[144:147], v250, v195 op_sel_hi:[0,0,0]
	v_mfma_scale_f32_16x16x128_f8f6f4 v[136:139], v[196:203], v[24:31], v[136:139], v250, v195 op_sel_hi:[0,0,0]
	v_mfma_scale_f32_16x16x128_f8f6f4 v[128:131], v[204:211], v[24:31], v[128:131], v250, v195 op_sel_hi:[0,0,0]
	v_mfma_scale_f32_16x16x128_f8f6f4 v[124:127], v[196:203], v[16:23], v[124:127], v250, v195 op_sel_hi:[0,0,0]
	v_mfma_scale_f32_16x16x128_f8f6f4 v[116:119], v[204:211], v[16:23], v[116:119], v250, v195 op_sel_hi:[0,0,0]
	s_setprio 0
	v_mov_b32_e32 v178, v184
	s_mov_b32 m0, s31
	s_barrier
	ds_read_b128 v[16:19], v194 offset:16384
	ds_read_b128 v[20:23], v194 offset:17408
	ds_read_b128 v[24:27], v194 offset:18432
	ds_read_b128 v[28:31], v194 offset:19456
	ds_read_b128 v[32:35], v194 offset:20480
	ds_read_b128 v[36:39], v194 offset:21504
	ds_read_b128 v[40:43], v194 offset:22528
	ds_read_b128 v[44:47], v194 offset:23552
	s_nop 0
	global_load_lds_dwordx4 v178, s[40:41]
	v_mov_b32_e32 v178, v185
	s_mov_b32 m0, s45
	s_nop 0
	global_load_lds_dwordx4 v178, s[40:41]
	s_barrier
	s_waitcnt lgkmcnt(0)
	s_setprio 1
	s_waitcnt lgkmcnt(0)
	v_mfma_scale_f32_16x16x128_f8f6f4 v[108:111], v[0:7], v[16:23], v[108:111], v250, v195 op_sel_hi:[0,0,0]
	v_mfma_scale_f32_16x16x128_f8f6f4 v[100:103], v[8:15], v[16:23], v[100:103], v250, v195 op_sel_hi:[0,0,0]
	v_mfma_scale_f32_16x16x128_f8f6f4 v[92:95], v[0:7], v[24:31], v[92:95], v250, v195 op_sel_hi:[0,0,0]
	v_mfma_scale_f32_16x16x128_f8f6f4 v[84:87], v[8:15], v[24:31], v[84:87], v250, v195 op_sel_hi:[0,0,0]
	v_mfma_scale_f32_16x16x128_f8f6f4 v[76:79], v[0:7], v[32:39], v[76:79], v250, v195 op_sel_hi:[0,0,0]
	v_mfma_scale_f32_16x16x128_f8f6f4 v[68:71], v[8:15], v[32:39], v[68:71], v250, v195 op_sel_hi:[0,0,0]
	v_mfma_scale_f32_16x16x128_f8f6f4 v[60:63], v[0:7], v[40:47], v[60:63], v250, v195 op_sel_hi:[0,0,0]
	v_mfma_scale_f32_16x16x128_f8f6f4 v[52:55], v[8:15], v[40:47], v[52:55], v250, v195 op_sel_hi:[0,0,0]
	s_setprio 0
	s_barrier
	s_add_u32 s62, s38, 0x40000
	s_addc_u32 s63, s39, 0
	v_mov_b32_e32 v0, v181
	s_add_i32 s61, s5, s42
	s_mov_b32 m0, s61
	s_nop 0
	global_load_lds_dwordx4 v0, s[62:63]
	v_mov_b32_e32 v0, v183
	s_add_i32 m0, s61, 0x2000
	s_nop 0
	global_load_lds_dwordx4 v0, s[62:63]
	s_waitcnt vmcnt(6)
	s_barrier
	s_setprio 1
	v_mfma_scale_f32_16x16x128_f8f6f4 v[104:107], v[196:203], v[16:23], v[104:107], v250, v195 op_sel_hi:[0,0,0]
	v_mfma_scale_f32_16x16x128_f8f6f4 v[96:99], v[204:211], v[16:23], v[96:99], v250, v195 op_sel_hi:[0,0,0]
	v_mfma_scale_f32_16x16x128_f8f6f4 v[88:91], v[196:203], v[24:31], v[88:91], v250, v195 op_sel_hi:[0,0,0]
	v_mfma_scale_f32_16x16x128_f8f6f4 v[80:83], v[204:211], v[24:31], v[80:83], v250, v195 op_sel_hi:[0,0,0]
	v_mfma_scale_f32_16x16x128_f8f6f4 v[72:75], v[196:203], v[32:39], v[72:75], v250, v195 op_sel_hi:[0,0,0]
	v_mfma_scale_f32_16x16x128_f8f6f4 v[64:67], v[204:211], v[32:39], v[64:67], v250, v195 op_sel_hi:[0,0,0]
	v_mfma_scale_f32_16x16x128_f8f6f4 v[56:59], v[196:203], v[40:47], v[56:59], v250, v195 op_sel_hi:[0,0,0]
	v_mfma_scale_f32_16x16x128_f8f6f4 v[48:51], v[204:211], v[40:47], v[48:51], v250, v195 op_sel_hi:[0,0,0]
	s_setprio 0
	s_add_i32 s61, 0, 0x18000
	v_add_u32_e32 v12, s61, v188
	s_barrier
	ds_read_b128 v[0:3], v12
	ds_read_b128 v[4:7], v12 offset:1024
	ds_read_b128 v[8:11], v12 offset:2048
	ds_read_b128 v[12:15], v12 offset:3072
	v_mov_b32_e32 v178, v186
	s_mov_b32 m0, s46
	ds_read_b128 v[16:19], v194 offset:32768
	ds_read_b128 v[20:23], v194 offset:33792
	ds_read_b128 v[24:27], v194 offset:34816
	ds_read_b128 v[28:31], v194 offset:35840
	ds_read_b128 v[32:35], v194 offset:36864
	ds_read_b128 v[36:39], v194 offset:37888
	ds_read_b128 v[40:43], v194 offset:38912
	ds_read_b128 v[44:47], v194 offset:39936
	s_nop 0
	global_load_lds_dwordx4 v178, s[40:41]
	v_mov_b32_e32 v178, v187
	s_mov_b32 m0, s47
	s_nop 0
	global_load_lds_dwordx4 v178, s[40:41]
	s_waitcnt lgkmcnt(8)
	s_barrier
	s_waitcnt lgkmcnt(0)
	s_setprio 1
	s_waitcnt lgkmcnt(0)
	v_mfma_scale_f32_16x16x128_f8f6f4 v[172:175], v[0:7], v[16:23], v[172:175], v250, v195 op_sel_hi:[0,0,0]
	v_mfma_scale_f32_16x16x128_f8f6f4 v[168:171], v[8:15], v[16:23], v[168:171], v250, v195 op_sel_hi:[0,0,0]
	v_mfma_scale_f32_16x16x128_f8f6f4 v[164:167], v[0:7], v[24:31], v[164:167], v250, v195 op_sel_hi:[0,0,0]
	v_mfma_scale_f32_16x16x128_f8f6f4 v[156:159], v[8:15], v[24:31], v[156:159], v250, v195 op_sel_hi:[0,0,0]
	v_mfma_scale_f32_16x16x128_f8f6f4 v[140:143], v[0:7], v[32:39], v[140:143], v250, v195 op_sel_hi:[0,0,0]
	v_mfma_scale_f32_16x16x128_f8f6f4 v[132:135], v[8:15], v[32:39], v[132:135], v250, v195 op_sel_hi:[0,0,0]
	v_mfma_scale_f32_16x16x128_f8f6f4 v[120:123], v[0:7], v[40:47], v[120:123], v250, v195 op_sel_hi:[0,0,0]
	v_mfma_scale_f32_16x16x128_f8f6f4 v[112:115], v[8:15], v[40:47], v[112:115], v250, v195 op_sel_hi:[0,0,0]
	s_setprio 0
	s_barrier
	s_add_i32 s62, 0, 0x1c000
	v_add_u32_e32 v178, s62, v188
	ds_read_b128 v[196:199], v178
	ds_read_b128 v[200:203], v178 offset:1024
	ds_read_b128 v[204:207], v178 offset:2048
	ds_read_b128 v[208:211], v178 offset:3072
	v_mov_b32_e32 v178, v181
	s_add_i32 s61, s61, s42
	v_lshl_add_u64 v[212:213], s[38:39], 0, v[178:179]
	v_lshl_add_u64 v[212:213], v[212:213], 0, s[12:13]
	s_mov_b32 m0, s61
	v_mov_b32_e32 v178, v183
	global_load_lds_dwordx4 v[212:213], off
	s_add_i32 m0, s61, 0x2000
	v_lshl_add_u64 v[212:213], s[38:39], 0, v[178:179]
	v_lshl_add_u64 v[212:213], v[212:213], 0, s[12:13]
	global_load_lds_dwordx4 v[212:213], off
	s_barrier
	s_waitcnt lgkmcnt(0)
	s_setprio 1
	s_waitcnt lgkmcnt(0)
	v_mfma_scale_f32_16x16x128_f8f6f4 v[160:163], v[196:203], v[16:23], v[160:163], v250, v195 op_sel_hi:[0,0,0]
	v_mfma_scale_f32_16x16x128_f8f6f4 v[152:155], v[204:211], v[16:23], v[152:155], v250, v195 op_sel_hi:[0,0,0]
	v_mfma_scale_f32_16x16x128_f8f6f4 v[148:151], v[196:203], v[24:31], v[148:151], v250, v195 op_sel_hi:[0,0,0]
	v_mfma_scale_f32_16x16x128_f8f6f4 v[144:147], v[204:211], v[24:31], v[144:147], v250, v195 op_sel_hi:[0,0,0]
	v_mfma_scale_f32_16x16x128_f8f6f4 v[136:139], v[196:203], v[32:39], v[136:139], v250, v195 op_sel_hi:[0,0,0]
	v_mfma_scale_f32_16x16x128_f8f6f4 v[128:131], v[204:211], v[32:39], v[128:131], v250, v195 op_sel_hi:[0,0,0]
	v_mfma_scale_f32_16x16x128_f8f6f4 v[124:127], v[196:203], v[40:47], v[124:127], v250, v195 op_sel_hi:[0,0,0]
	v_mfma_scale_f32_16x16x128_f8f6f4 v[116:119], v[204:211], v[40:47], v[116:119], v250, v195 op_sel_hi:[0,0,0]
	s_setprio 0
	v_mov_b32_e32 v178, v184
	s_barrier
	ds_read_b128 v[16:19], v194 offset:49152
	ds_read_b128 v[20:23], v194 offset:50176
	ds_read_b128 v[24:27], v194 offset:51200
	ds_read_b128 v[28:31], v194 offset:52224
	ds_read_b128 v[32:35], v194 offset:53248
	ds_read_b128 v[36:39], v194 offset:54272
	ds_read_b128 v[40:43], v194 offset:55296
	ds_read_b128 v[44:47], v194 offset:56320
	s_mov_b32 m0, s52
	v_lshl_add_u64 v[212:213], s[40:41], 0, v[178:179]
	v_lshl_add_u64 v[212:213], v[212:213], 0, s[12:13]
	v_mov_b32_e32 v178, v185
	global_load_lds_dwordx4 v[212:213], off
	s_mov_b32 m0, s53
	v_lshl_add_u64 v[212:213], s[40:41], 0, v[178:179]
	v_lshl_add_u64 v[212:213], v[212:213], 0, s[12:13]
	global_load_lds_dwordx4 v[212:213], off
	s_barrier
	s_waitcnt lgkmcnt(0)
	s_setprio 1
	s_waitcnt lgkmcnt(0)
	v_mfma_scale_f32_16x16x128_f8f6f4 v[108:111], v[0:7], v[16:23], v[108:111], v250, v195 op_sel_hi:[0,0,0]
	v_mfma_scale_f32_16x16x128_f8f6f4 v[100:103], v[8:15], v[16:23], v[100:103], v250, v195 op_sel_hi:[0,0,0]
	v_mfma_scale_f32_16x16x128_f8f6f4 v[92:95], v[0:7], v[24:31], v[92:95], v250, v195 op_sel_hi:[0,0,0]
	v_mfma_scale_f32_16x16x128_f8f6f4 v[84:87], v[8:15], v[24:31], v[84:87], v250, v195 op_sel_hi:[0,0,0]
	v_mfma_scale_f32_16x16x128_f8f6f4 v[76:79], v[0:7], v[32:39], v[76:79], v250, v195 op_sel_hi:[0,0,0]
	v_mfma_scale_f32_16x16x128_f8f6f4 v[68:71], v[8:15], v[32:39], v[68:71], v250, v195 op_sel_hi:[0,0,0]
	v_mfma_scale_f32_16x16x128_f8f6f4 v[60:63], v[0:7], v[40:47], v[60:63], v250, v195 op_sel_hi:[0,0,0]
	v_mfma_scale_f32_16x16x128_f8f6f4 v[52:55], v[8:15], v[40:47], v[52:55], v250, v195 op_sel_hi:[0,0,0]
	s_setprio 0
	s_barrier
	s_add_u32 s38, s38, 0x40080
	s_addc_u32 s39, s39, 0
	v_mov_b32_e32 v0, v181
	s_add_i32 s40, s62, s42
	s_mov_b32 m0, s40
	s_nop 0
	global_load_lds_dwordx4 v0, s[38:39]
	v_mov_b32_e32 v0, v183
	s_add_i32 m0, s40, 0x2000
	s_nop 0
	global_load_lds_dwordx4 v0, s[38:39]
	s_waitcnt vmcnt(6)
	s_barrier
	s_setprio 1
	v_mfma_scale_f32_16x16x128_f8f6f4 v[104:107], v[196:203], v[16:23], v[104:107], v250, v195 op_sel_hi:[0,0,0]
	v_mfma_scale_f32_16x16x128_f8f6f4 v[96:99], v[204:211], v[16:23], v[96:99], v250, v195 op_sel_hi:[0,0,0]
	v_mfma_scale_f32_16x16x128_f8f6f4 v[88:91], v[196:203], v[24:31], v[88:91], v250, v195 op_sel_hi:[0,0,0]
	v_mfma_scale_f32_16x16x128_f8f6f4 v[80:83], v[204:211], v[24:31], v[80:83], v250, v195 op_sel_hi:[0,0,0]
	v_mfma_scale_f32_16x16x128_f8f6f4 v[72:75], v[196:203], v[32:39], v[72:75], v250, v195 op_sel_hi:[0,0,0]
	v_mfma_scale_f32_16x16x128_f8f6f4 v[64:67], v[204:211], v[32:39], v[64:67], v250, v195 op_sel_hi:[0,0,0]
	v_mfma_scale_f32_16x16x128_f8f6f4 v[56:59], v[196:203], v[40:47], v[56:59], v250, v195 op_sel_hi:[0,0,0]
	v_mfma_scale_f32_16x16x128_f8f6f4 v[48:51], v[204:211], v[40:47], v[48:51], v250, v195 op_sel_hi:[0,0,0]
	s_setprio 0
	s_add_i32 s60, s60, 2
	s_add_u32 s36, s36, 0x100
	s_addc_u32 s37, s37, 0
	s_add_u32 s8, s8, 0x100
	s_addc_u32 s23, s23, 0
	s_cmp_gt_u32 s60, 13
	s_barrier
	s_cbranch_scc1 .LBB0_1936

.Lpeelg_t0:
	s_add_u32 s40, s36, 0x80
	s_addc_u32 s41, s37, 0
	v_add_u32_e32 v178, s5, v188
	s_and_b64 s[38:39], s[38:39], exec
	ds_read_b128 v[196:199], v178
	ds_read_b128 v[200:203], v178 offset:1024
	ds_read_b128 v[204:207], v178 offset:2048
	ds_read_b128 v[208:211], v178 offset:3072
	v_mov_b32_e32 v178, v181
	s_mov_b32 m0, s43
	s_cselect_b32 s39, s27, s23
	s_cselect_b32 s38, s26, s8
	s_waitcnt lgkmcnt(0)
	v_mfma_scale_f32_16x16x128_f8f6f4 v[172:175], v[0:7], v[40:47], 0, v250, v195 op_sel_hi:[0,0,0]
	global_load_lds_dwordx4 v178, s[38:39]
	v_mov_b32_e32 v178, v183
	s_mov_b32 m0, s44
	s_cselect_b32 s41, s11, s41
	global_load_lds_dwordx4 v178, s[38:39]
	v_mfma_scale_f32_16x16x128_f8f6f4 v[168:171], v[8:15], v[40:47], 0, v250, v195 op_sel_hi:[0,0,0]
	s_barrier
	s_waitcnt lgkmcnt(0)
	s_cselect_b32 s40, s10, s40
	v_mfma_scale_f32_16x16x128_f8f6f4 v[164:167], v[0:7], v[32:39], 0, v250, v195 op_sel_hi:[0,0,0]
	v_mfma_scale_f32_16x16x128_f8f6f4 v[156:159], v[8:15], v[32:39], 0, v250, v195 op_sel_hi:[0,0,0]
	v_mfma_scale_f32_16x16x128_f8f6f4 v[140:143], v[0:7], v[24:31], 0, v250, v195 op_sel_hi:[0,0,0]
	v_mfma_scale_f32_16x16x128_f8f6f4 v[132:135], v[8:15], v[24:31], 0, v250, v195 op_sel_hi:[0,0,0]
	v_mfma_scale_f32_16x16x128_f8f6f4 v[120:123], v[0:7], v[16:23], 0, v250, v195 op_sel_hi:[0,0,0]
	v_mfma_scale_f32_16x16x128_f8f6f4 v[112:115], v[8:15], v[16:23], 0, v250, v195 op_sel_hi:[0,0,0]
	s_setprio 1
	v_mfma_scale_f32_16x16x128_f8f6f4 v[160:163], v[196:203], v[40:47], 0, v250, v195 op_sel_hi:[0,0,0]
	v_mfma_scale_f32_16x16x128_f8f6f4 v[152:155], v[204:211], v[40:47], 0, v250, v195 op_sel_hi:[0,0,0]
	v_mfma_scale_f32_16x16x128_f8f6f4 v[148:151], v[196:203], v[32:39], 0, v250, v195 op_sel_hi:[0,0,0]
	v_mfma_scale_f32_16x16x128_f8f6f4 v[144:147], v[204:211], v[32:39], 0, v250, v195 op_sel_hi:[0,0,0]
	v_mfma_scale_f32_16x16x128_f8f6f4 v[136:139], v[196:203], v[24:31], 0, v250, v195 op_sel_hi:[0,0,0]
	v_mfma_scale_f32_16x16x128_f8f6f4 v[128:131], v[204:211], v[24:31], 0, v250, v195 op_sel_hi:[0,0,0]
	v_mfma_scale_f32_16x16x128_f8f6f4 v[124:127], v[196:203], v[16:23], 0, v250, v195 op_sel_hi:[0,0,0]
	v_mfma_scale_f32_16x16x128_f8f6f4 v[116:119], v[204:211], v[16:23], 0, v250, v195 op_sel_hi:[0,0,0]
	s_setprio 0
	v_mov_b32_e32 v178, v184
	s_mov_b32 m0, s31
	s_barrier
	ds_read_b128 v[16:19], v194 offset:16384
	ds_read_b128 v[20:23], v194 offset:17408
	ds_read_b128 v[24:27], v194 offset:18432
	ds_read_b128 v[28:31], v194 offset:19456
	ds_read_b128 v[32:35], v194 offset:20480
	ds_read_b128 v[36:39], v194 offset:21504
	ds_read_b128 v[40:43], v194 offset:22528
	ds_read_b128 v[44:47], v194 offset:23552
	s_nop 0
	global_load_lds_dwordx4 v178, s[40:41]
	v_mov_b32_e32 v178, v185
	s_mov_b32 m0, s45
	s_nop 0
	global_load_lds_dwordx4 v178, s[40:41]
	s_barrier
	s_waitcnt lgkmcnt(0)
	s_setprio 1
	s_waitcnt lgkmcnt(0)
	v_mfma_scale_f32_16x16x128_f8f6f4 v[108:111], v[0:7], v[16:23], 0, v250, v195 op_sel_hi:[0,0,0]
	v_mfma_scale_f32_16x16x128_f8f6f4 v[100:103], v[8:15], v[16:23], 0, v250, v195 op_sel_hi:[0,0,0]
	v_mfma_scale_f32_16x16x128_f8f6f4 v[92:95], v[0:7], v[24:31], 0, v250, v195 op_sel_hi:[0,0,0]
	v_mfma_scale_f32_16x16x128_f8f6f4 v[84:87], v[8:15], v[24:31], 0, v250, v195 op_sel_hi:[0,0,0]
	v_mfma_scale_f32_16x16x128_f8f6f4 v[76:79], v[0:7], v[32:39], 0, v250, v195 op_sel_hi:[0,0,0]
	v_mfma_scale_f32_16x16x128_f8f6f4 v[68:71], v[8:15], v[32:39], 0, v250, v195 op_sel_hi:[0,0,0]
	v_mfma_scale_f32_16x16x128_f8f6f4 v[60:63], v[0:7], v[40:47], 0, v250, v195 op_sel_hi:[0,0,0]
	v_mfma_scale_f32_16x16x128_f8f6f4 v[52:55], v[8:15], v[40:47], 0, v250, v195 op_sel_hi:[0,0,0]
	s_setprio 0
	s_barrier
	s_add_u32 s62, s38, 0x40000
	s_addc_u32 s63, s39, 0
	v_mov_b32_e32 v0, v181
	s_add_i32 s61, s5, s42
	s_mov_b32 m0, s61
	s_nop 0
	global_load_lds_dwordx4 v0, s[62:63]
	v_mov_b32_e32 v0, v183
	s_add_i32 m0, s61, 0x2000
	s_nop 0
	global_load_lds_dwordx4 v0, s[62:63]
	s_waitcnt vmcnt(6)
	s_barrier
	s_setprio 1
	v_mfma_scale_f32_16x16x128_f8f6f4 v[104:107], v[196:203], v[16:23], 0, v250, v195 op_sel_hi:[0,0,0]
	v_mfma_scale_f32_16x16x128_f8f6f4 v[96:99], v[204:211], v[16:23], 0, v250, v195 op_sel_hi:[0,0,0]
	v_mfma_scale_f32_16x16x128_f8f6f4 v[88:91], v[196:203], v[24:31], 0, v250, v195 op_sel_hi:[0,0,0]
	v_mfma_scale_f32_16x16x128_f8f6f4 v[80:83], v[204:211], v[24:31], 0, v250, v195 op_sel_hi:[0,0,0]
	v_mfma_scale_f32_16x16x128_f8f6f4 v[72:75], v[196:203], v[32:39], 0, v250, v195 op_sel_hi:[0,0,0]
	v_mfma_scale_f32_16x16x128_f8f6f4 v[64:67], v[204:211], v[32:39], 0, v250, v195 op_sel_hi:[0,0,0]
	v_mfma_scale_f32_16x16x128_f8f6f4 v[56:59], v[196:203], v[40:47], 0, v250, v195 op_sel_hi:[0,0,0]
	v_mfma_scale_f32_16x16x128_f8f6f4 v[48:51], v[204:211], v[40:47], 0, v250, v195 op_sel_hi:[0,0,0]
	s_setprio 0
	s_add_i32 s61, 0, 0x18000
	v_add_u32_e32 v12, s61, v188
	s_barrier
	ds_read_b128 v[0:3], v12
	ds_read_b128 v[4:7], v12 offset:1024
	ds_read_b128 v[8:11], v12 offset:2048
	ds_read_b128 v[12:15], v12 offset:3072
	v_mov_b32_e32 v178, v186
	s_mov_b32 m0, s46
	ds_read_b128 v[16:19], v194 offset:32768
	ds_read_b128 v[20:23], v194 offset:33792
	ds_read_b128 v[24:27], v194 offset:34816
	ds_read_b128 v[28:31], v194 offset:35840
	ds_read_b128 v[32:35], v194 offset:36864
	ds_read_b128 v[36:39], v194 offset:37888
	ds_read_b128 v[40:43], v194 offset:38912
	ds_read_b128 v[44:47], v194 offset:39936
	s_nop 0
	global_load_lds_dwordx4 v178, s[40:41]
	v_mov_b32_e32 v178, v187
	s_mov_b32 m0, s47
	s_nop 0
	global_load_lds_dwordx4 v178, s[40:41]
	s_waitcnt lgkmcnt(8)
	s_barrier
	s_waitcnt lgkmcnt(0)
	s_setprio 1
	s_waitcnt lgkmcnt(0)
	v_mfma_scale_f32_16x16x128_f8f6f4 v[172:175], v[0:7], v[16:23], v[172:175], v250, v195 op_sel_hi:[0,0,0]
	v_mfma_scale_f32_16x16x128_f8f6f4 v[168:171], v[8:15], v[16:23], v[168:171], v250, v195 op_sel_hi:[0,0,0]
	v_mfma_scale_f32_16x16x128_f8f6f4 v[164:167], v[0:7], v[24:31], v[164:167], v250, v195 op_sel_hi:[0,0,0]
	v_mfma_scale_f32_16x16x128_f8f6f4 v[156:159], v[8:15], v[24:31], v[156:159], v250, v195 op_sel_hi:[0,0,0]
	v_mfma_scale_f32_16x16x128_f8f6f4 v[140:143], v[0:7], v[32:39], v[140:143], v250, v195 op_sel_hi:[0,0,0]
	v_mfma_scale_f32_16x16x128_f8f6f4 v[132:135], v[8:15], v[32:39], v[132:135], v250, v195 op_sel_hi:[0,0,0]
	v_mfma_scale_f32_16x16x128_f8f6f4 v[120:123], v[0:7], v[40:47], v[120:123], v250, v195 op_sel_hi:[0,0,0]
	v_mfma_scale_f32_16x16x128_f8f6f4 v[112:115], v[8:15], v[40:47], v[112:115], v250, v195 op_sel_hi:[0,0,0]
	s_setprio 0
	s_barrier
	s_add_i32 s62, 0, 0x1c000
	v_add_u32_e32 v178, s62, v188
	ds_read_b128 v[196:199], v178
	ds_read_b128 v[200:203], v178 offset:1024
	ds_read_b128 v[204:207], v178 offset:2048
	ds_read_b128 v[208:211], v178 offset:3072
	v_mov_b32_e32 v178, v181
	s_add_i32 s61, s61, s42
	v_lshl_add_u64 v[212:213], s[38:39], 0, v[178:179]
	v_lshl_add_u64 v[212:213], v[212:213], 0, s[12:13]
	s_mov_b32 m0, s61
	v_mov_b32_e32 v178, v183
	global_load_lds_dwordx4 v[212:213], off
	s_add_i32 m0, s61, 0x2000
	v_lshl_add_u64 v[212:213], s[38:39], 0, v[178:179]
	v_lshl_add_u64 v[212:213], v[212:213], 0, s[12:13]
	global_load_lds_dwordx4 v[212:213], off
	s_barrier
	s_waitcnt lgkmcnt(0)
	s_setprio 1
	s_waitcnt lgkmcnt(0)
	v_mfma_scale_f32_16x16x128_f8f6f4 v[160:163], v[196:203], v[16:23], v[160:163], v250, v195 op_sel_hi:[0,0,0]
	v_mfma_scale_f32_16x16x128_f8f6f4 v[152:155], v[204:211], v[16:23], v[152:155], v250, v195 op_sel_hi:[0,0,0]
	v_mfma_scale_f32_16x16x128_f8f6f4 v[148:151], v[196:203], v[24:31], v[148:151], v250, v195 op_sel_hi:[0,0,0]
	v_mfma_scale_f32_16x16x128_f8f6f4 v[144:147], v[204:211], v[24:31], v[144:147], v250, v195 op_sel_hi:[0,0,0]
	v_mfma_scale_f32_16x16x128_f8f6f4 v[136:139], v[196:203], v[32:39], v[136:139], v250, v195 op_sel_hi:[0,0,0]
	v_mfma_scale_f32_16x16x128_f8f6f4 v[128:131], v[204:211], v[32:39], v[128:131], v250, v195 op_sel_hi:[0,0,0]
	v_mfma_scale_f32_16x16x128_f8f6f4 v[124:127], v[196:203], v[40:47], v[124:127], v250, v195 op_sel_hi:[0,0,0]
	v_mfma_scale_f32_16x16x128_f8f6f4 v[116:119], v[204:211], v[40:47], v[116:119], v250, v195 op_sel_hi:[0,0,0]
	s_setprio 0
	v_mov_b32_e32 v178, v184
	s_barrier
	ds_read_b128 v[16:19], v194 offset:49152
	ds_read_b128 v[20:23], v194 offset:50176
	ds_read_b128 v[24:27], v194 offset:51200
	ds_read_b128 v[28:31], v194 offset:52224
	ds_read_b128 v[32:35], v194 offset:53248
	ds_read_b128 v[36:39], v194 offset:54272
	ds_read_b128 v[40:43], v194 offset:55296
	ds_read_b128 v[44:47], v194 offset:56320
	s_mov_b32 m0, s52
	v_lshl_add_u64 v[212:213], s[40:41], 0, v[178:179]
	v_lshl_add_u64 v[212:213], v[212:213], 0, s[12:13]
	v_mov_b32_e32 v178, v185
	global_load_lds_dwordx4 v[212:213], off
	s_mov_b32 m0, s53
	v_lshl_add_u64 v[212:213], s[40:41], 0, v[178:179]
	v_lshl_add_u64 v[212:213], v[212:213], 0, s[12:13]
	global_load_lds_dwordx4 v[212:213], off
	s_barrier
	s_waitcnt lgkmcnt(0)
	s_setprio 1
	s_waitcnt lgkmcnt(0)
	v_mfma_scale_f32_16x16x128_f8f6f4 v[108:111], v[0:7], v[16:23], v[108:111], v250, v195 op_sel_hi:[0,0,0]
	v_mfma_scale_f32_16x16x128_f8f6f4 v[100:103], v[8:15], v[16:23], v[100:103], v250, v195 op_sel_hi:[0,0,0]
	v_mfma_scale_f32_16x16x128_f8f6f4 v[92:95], v[0:7], v[24:31], v[92:95], v250, v195 op_sel_hi:[0,0,0]
	v_mfma_scale_f32_16x16x128_f8f6f4 v[84:87], v[8:15], v[24:31], v[84:87], v250, v195 op_sel_hi:[0,0,0]
	v_mfma_scale_f32_16x16x128_f8f6f4 v[76:79], v[0:7], v[32:39], v[76:79], v250, v195 op_sel_hi:[0,0,0]
	v_mfma_scale_f32_16x16x128_f8f6f4 v[68:71], v[8:15], v[32:39], v[68:71], v250, v195 op_sel_hi:[0,0,0]
	v_mfma_scale_f32_16x16x128_f8f6f4 v[60:63], v[0:7], v[40:47], v[60:63], v250, v195 op_sel_hi:[0,0,0]
	v_mfma_scale_f32_16x16x128_f8f6f4 v[52:55], v[8:15], v[40:47], v[52:55], v250, v195 op_sel_hi:[0,0,0]
	s_setprio 0
	s_barrier
	s_add_u32 s38, s38, 0x40080
	s_addc_u32 s39, s39, 0
	v_mov_b32_e32 v0, v181
	s_add_i32 s40, s62, s42
	s_mov_b32 m0, s40
	s_nop 0
	global_load_lds_dwordx4 v0, s[38:39]
	v_mov_b32_e32 v0, v183
	s_add_i32 m0, s40, 0x2000
	s_nop 0
	global_load_lds_dwordx4 v0, s[38:39]
	s_waitcnt vmcnt(6)
	s_barrier
	s_setprio 1
	v_mfma_scale_f32_16x16x128_f8f6f4 v[104:107], v[196:203], v[16:23], v[104:107], v250, v195 op_sel_hi:[0,0,0]
	v_mfma_scale_f32_16x16x128_f8f6f4 v[96:99], v[204:211], v[16:23], v[96:99], v250, v195 op_sel_hi:[0,0,0]
	v_mfma_scale_f32_16x16x128_f8f6f4 v[88:91], v[196:203], v[24:31], v[88:91], v250, v195 op_sel_hi:[0,0,0]
	v_mfma_scale_f32_16x16x128_f8f6f4 v[80:83], v[204:211], v[24:31], v[80:83], v250, v195 op_sel_hi:[0,0,0]
	v_mfma_scale_f32_16x16x128_f8f6f4 v[72:75], v[196:203], v[32:39], v[72:75], v250, v195 op_sel_hi:[0,0,0]
	v_mfma_scale_f32_16x16x128_f8f6f4 v[64:67], v[204:211], v[32:39], v[64:67], v250, v195 op_sel_hi:[0,0,0]
	v_mfma_scale_f32_16x16x128_f8f6f4 v[56:59], v[196:203], v[40:47], v[56:59], v250, v195 op_sel_hi:[0,0,0]
	v_mfma_scale_f32_16x16x128_f8f6f4 v[48:51], v[204:211], v[40:47], v[48:51], v250, v195 op_sel_hi:[0,0,0]
	s_setprio 0
	s_add_i32 s60, s60, 2
	s_add_u32 s36, s36, 0x100
	s_addc_u32 s37, s37, 0
	s_add_u32 s8, s8, 0x100
	s_addc_u32 s23, s23, 0
	s_cmp_gt_u32 s60, 13
	s_barrier
	s_cbranch_scc1 .LBB0_1936
	s_branch .LBB0_1945
